# XCD-local grid barriers after phases 4,5,6,10 (next phase consumes same-XCD data only; runtime-checked bx%8==XCD grouping, falls back to full barrier)
# speedup vs baseline: 1.0030x; 1.0030x over previous
.LBB0_2:
	v_lshl_add_u32 v1, v0, 2, 0
	v_add_u32_e32 v1, 0x20000, v1
	v_mov_b32_e32 v2, 0
	ds_write2st64_b32 v1, v2, v2 offset1:8
	ds_write2st64_b32 v1, v2, v2 offset0:16 offset1:24
	v_or_b32_e32 v1, 0x800, v0
	s_mov_b64 s[0:1], -1
	s_and_saveexec_b64 s[2:3], s[0:1]
	v_lshl_add_u32 v3, v1, 2, 0
	v_add_u32_e32 v3, 0x20000, v3
	ds_write_b32 v3, v2
	s_or_b64 exec, exec, s[2:3]
	s_and_saveexec_b64 s[2:3], s[0:1]
	s_add_i32 s0, 0, 0x20000
	v_lshl_add_u32 v1, v1, 2, s0
	v_mov_b32_e32 v2, 0
	ds_write_b32 v1, v2 offset:2048
	s_or_b64 exec, exec, s[2:3]
	v_or_b32_e32 v1, 0xc00, v0
	v_cmp_gt_u32_e64 s[0:1], 7, 6
	v_cmp_gt_u32_e64 s[4:5], 7, 5
	s_and_saveexec_b64 s[2:3], s[4:5]
	v_lshl_add_u32 v2, v1, 2, 0
	v_add_u32_e32 v2, 0x20000, v2
	v_mov_b32_e32 v3, 0
	ds_write_b32 v2, v3
	s_or_b64 exec, exec, s[2:3]
	s_and_saveexec_b64 s[2:3], s[0:1]
	s_add_i32 s0, 0, 0x20000
	v_lshl_add_u32 v1, v1, 2, s0
	v_mov_b32_e32 v2, 0
	ds_write_b32 v1, v2 offset:2048
	s_or_b64 exec, exec, s[2:3]
	v_readlane_b32 s0, v252, 0
	v_readlane_b32 s1, v252, 1
	s_waitcnt lgkmcnt(0)
	s_barrier
	s_load_dwordx2 s[88:89], s[0:1], 0xa0
	s_mov_b32 s46, 0
	s_waitcnt lgkmcnt(0)
	s_sub_i32 s0, s89, s88
	s_cmp_lt_i32 s0, 2
	s_mov_b32 s0, 0
	v_writelane_b32 v252, s0, 4
	s_cbranch_scc1 .LBB0_15
	s_getreg_b32 s0, hwreg(HW_REG_XCC_ID, 0, 4)
	v_cmp_eq_u32_e32 vcc, 0, v0
	s_and_b32 s46, s0, 15
	s_and_saveexec_b64 s[0:1], vcc
	s_cbranch_execz .LBB0_14
	s_mov_b64 s[2:3], exec
	v_mbcnt_lo_u32_b32 v0, s2, 0
	v_mbcnt_hi_u32_b32 v0, s3, v0
	v_cmp_eq_u32_e32 vcc, 0, v0
	s_and_b64 s[4:5], exec, vcc
	s_mov_b64 exec, s[4:5]
	s_cbranch_execz .LBB0_14
	v_readlane_b32 s4, v252, 0
	v_readlane_b32 s5, v252, 1
	s_load_dwordx2 s[4:5], s[4:5], 0x98
	s_lshl_b32 s6, s46, 8
	v_mov_b32_e32 v0, 0x4000
	s_waitcnt lgkmcnt(0)
	s_and_b32 s7, s92, 7
	s_lshl_b32 s7, s7, 3
	s_and_b32 s8, s46, 7
	s_add_i32 s7, s7, s8
	s_lshl_b64 s[8:9], 1, s7
	s_cmp_gt_u32 s46, 7
	s_cselect_b32 s8, -1, s8
	v_mov_b32_e32 v4, s8
	v_mov_b32_e32 v5, s9
	v_mov_b32_e32 v3, 0x8000
	global_atomic_or_x2 v3, v[4:5], s[4:5]
	s_add_u32 s4, s4, s6
	s_addc_u32 s5, s5, 0
	s_bcnt1_i32_b64 s2, s[2:3]
	v_mov_b32_e32 v1, s2
	global_atomic_add v0, v1, s[4:5] offset:1024

.LBB0_1116:
	s_andn2_saveexec_b64 s[8:9], s[8:9]
	s_cbranch_execz .LBB0_1134
	s_mov_b64 s[8:9], exec
	v_mov_b32_e32 v4, 0x8000
	global_load_dwordx2 v[4:5], v4, s[4:5] sc1
	buffer_wbl2 sc1
	s_waitcnt lgkmcnt(0)
	s_waitcnt vmcnt(0)
	v_readfirstlane_b32 s10, v4
	v_readfirstlane_b32 s11, v5
	s_sub_u32 s12, s10, 0x1010101
	s_subb_u32 s13, s11, 0x1010101
	s_and_b64 s[12:13], s[12:13], s[10:11]
	s_cmp_eq_u64 s[12:13], 0
	s_cbranch_scc0 .Lfull_seam5
	s_mov_b64 s[4:5], exec
	s_branch .LBB0_1133
.Lfull_seam5:
	v_mbcnt_lo_u32_b32 v1, s8, 0
	v_mbcnt_hi_u32_b32 v1, s9, v1
	v_cmp_eq_u32_e32 vcc, 0, v1
	s_and_saveexec_b64 s[10:11], vcc
	s_cbranch_execz .LBB0_1119
	s_bcnt1_i32_b64 s8, s[8:9]
	v_mov_b32_e32 v2, s8
	v_mov_b32_e32 v3, 0x7000
	global_atomic_add v2, v3, v2, s[4:5] offset:1024 sc0

.LBB0_1717:
	s_mov_b64 s[8:9], exec
	v_mov_b32_e32 v4, 0x8000
	global_load_dwordx2 v[4:5], v4, s[4:5] sc1
	buffer_wbl2 sc1
	s_waitcnt lgkmcnt(0)
	s_waitcnt vmcnt(0)
	v_readfirstlane_b32 s10, v4
	v_readfirstlane_b32 s11, v5
	s_sub_u32 s12, s10, 0x1010101
	s_subb_u32 s13, s11, 0x1010101
	s_and_b64 s[12:13], s[12:13], s[10:11]
	s_cmp_eq_u64 s[12:13], 0
	s_cbranch_scc0 .Lfull_seam11
	s_mov_b64 s[4:5], exec
	s_branch .Lloc_far11

.Lloc_far11:
	s_getpc_b64 s[98:99]
